# speedup vs baseline: 1.0086x; 1.0086x over previous
amdhsa.kernels:
  - .agpr_count:     0
    .args:
      - .actual_access:  read_only
        .address_space:  global
        .offset:         0
        .size:           8
        .value_kind:     global_buffer
      - .actual_access:  read_only
        .address_space:  global
        .offset:         8
        .size:           8
        .value_kind:     global_buffer
      - .actual_access:  read_only
        .address_space:  global
        .offset:         16
        .size:           8
        .value_kind:     global_buffer
      - .actual_access:  write_only
        .address_space:  global
        .offset:         24
        .size:           8
        .value_kind:     global_buffer
      - .actual_access:  write_only
        .address_space:  global
        .offset:         32
        .size:           8
        .value_kind:     global_buffer
      - .actual_access:  write_only
        .address_space:  global
        .offset:         40
        .size:           8
        .value_kind:     global_buffer
      - .actual_access:  read_only
        .address_space:  global
        .offset:         48
        .size:           8
        .value_kind:     global_buffer
      - .actual_access:  write_only
        .address_space:  global
        .offset:         56
        .size:           8
        .value_kind:     global_buffer
    .group_segment_fixed_size: 24576
    .kernarg_segment_align: 8
    .kernarg_segment_size: 64
    .language:       OpenCL C
    .language_version:
      - 2
      - 0
    .max_flat_workgroup_size: 512
    .name:           _Z11prep_kernelPKfS0_S0_PDF16_PfPiS0_S1_
    .private_segment_fixed_size: 0
    .sgpr_count:     102
    .sgpr_spill_count: 0
    .symbol:         _Z11prep_kernelPKfS0_S0_PDF16_PfPiS0_S1_.kd
    .uniform_work_group_size: 1
    .uses_dynamic_stack: false
    .vgpr_count:     160
    .vgpr_spill_count: 0
    .wavefront_size: 64
  - .agpr_count:     256
    .args:
      - .actual_access:  read_only
        .address_space:  global
        .offset:         0
        .size:           8
        .value_kind:     global_buffer
      - .actual_access:  read_only
        .address_space:  global
        .offset:         8
        .size:           8
        .value_kind:     global_buffer
      - .actual_access:  read_only
        .address_space:  global
        .offset:         16
        .size:           8
        .value_kind:     global_buffer
      - .actual_access:  write_only
        .address_space:  global
        .offset:         24
        .size:           8
        .value_kind:     global_buffer
      - .actual_access:  read_only
        .address_space:  global
        .offset:         32
        .size:           8
        .value_kind:     global_buffer
    .group_segment_fixed_size: 148624
    .kernarg_segment_align: 8
    .kernarg_segment_size: 40
    .language:       OpenCL C
    .language_version:
      - 2
      - 0
    .max_flat_workgroup_size: 256
    .name:           _Z10ode_kernelPKfPKDF16_S2_PfPKi
    .private_segment_fixed_size: 0
    .sgpr_count:     59
    .sgpr_spill_count: 0
    .symbol:         _Z10ode_kernelPKfPKDF16_S2_PfPKi.kd
    .uniform_work_group_size: 1
    .uses_dynamic_stack: false
    .vgpr_count:     512
    .vgpr_spill_count: 0
    .wavefront_size: 64
